# odd-layer row-quantisation block: sums-of-squares entry requested before the 16 row loads (same reordering as the even-layer one)
# baseline (speedup 1.0000x reference)
; __device__ __forceinline__ float shfl_xor_f(float v, int mask, int lane) { return __int_as_float(__builtin_amdgcn_ds_bpermute((lane ^ mask) << 2, __float_as_int(v))); }
; __device__ __forceinline__ void quant_rows(unsigned char* ws, size_t xq_off, size_t sar_off, int gw, int NGW, int lane) {
;     const bf16_t* xb = (const bf16_t*)(ws + WS_XB); signed char* xq = (signed char*)(ws + xq_off); float* sar = (float*)(ws + sar_off); const float* ssp = (const float*)(ws + WS_SSP);
;     for (int m = gw; m < M; m += 8 * NGW) {
;         u32x4 a[8][2]; float mx[8];
; #pragma unroll
;         for (int q = 0; q < 8; ++q) { const u32x4* p = (const u32x4*)(xb + (size_t)(m + q * NGW) * D + 16 * lane); a[q][0] = p[0]; a[q][1] = p[1]; }
;         float ssv = 0.f;
;         if (lane < 32) { const f32x4 s4 = *(const f32x4*)(ssp + (size_t)(m + (lane >> 2) * NGW) * 16 + 4 * (lane & 3)); ssv = (s4[0] + s4[1]) + (s4[2] + s4[3]); }
;         ssv += shfl_xor_f(ssv, 1, lane); ssv += shfl_xor_f(ssv, 2, lane);
.LBB0_222:
	s_waitcnt lgkmcnt(0)
	v_mov_b32_e32 v73, 0
	v_add_u32_e32 v72, s26, v74
	s_and_saveexec_b64 s[24:25], s[4:5]
	v_ashrrev_i32_e32 v73, 31, v72
	v_lshlrev_b64 v[80:81], 6, v[72:73]
	v_lshl_add_u64 v[80:81], v[68:69], 0, v[80:81]
	global_load_dwordx4 v[80:83], v[80:81], off
	s_or_b64 exec, exec, s[24:25]
	s_ashr_i32 s27, s26, 31
	s_add_i32 s46, s26, s1
	s_lshl_b64 s[24:25], s[26:27], 11
	s_ashr_i32 s47, s46, 31
	s_add_i32 s30, s2, s26
	v_lshl_add_u64 v[2:3], v[66:67], 0, s[24:25]
	s_lshl_b64 s[24:25], s[46:47], 11
	s_ashr_i32 s31, s30, 31
	global_load_dwordx4 v[58:61], v[2:3], off offset:16
	global_load_dwordx4 v[62:65], v[2:3], off
	v_lshl_add_u64 v[2:3], v[66:67], 0, s[24:25]
	s_lshl_b64 s[24:25], s[30:31], 11
	global_load_dwordx4 v[50:53], v[2:3], off offset:16
	global_load_dwordx4 v[54:57], v[2:3], off
	v_lshl_add_u64 v[2:3], v[66:67], 0, s[24:25]
	global_load_dwordx4 v[42:45], v[2:3], off offset:16
	global_load_dwordx4 v[46:49], v[2:3], off
	s_load_dword s28, s[82:83], 0x0
	s_add_i32 s36, s3, s26
	s_ashr_i32 s37, s36, 31
	s_waitcnt lgkmcnt(0)
	s_waitcnt lgkmcnt(0)
	s_mul_i32 s0, s28, 24
	s_add_i32 s34, s0, s26
	s_ashr_i32 s35, s34, 31
	s_mul_i32 s0, s28, 40
	s_lshl_b64 s[24:25], s[34:35], 11
	s_add_i32 s38, s0, s26
	s_mul_i32 s0, s28, 48
	v_lshl_add_u64 v[2:3], v[66:67], 0, s[24:25]
	s_lshl_b64 s[24:25], s[36:37], 11
	s_ashr_i32 s39, s38, 31
	s_add_i32 s48, s0, s26
	s_mul_i32 s0, s28, 56
	global_load_dwordx4 v[34:37], v[2:3], off offset:16
	global_load_dwordx4 v[38:41], v[2:3], off
	v_lshl_add_u64 v[2:3], v[66:67], 0, s[24:25]
	s_lshl_b64 s[24:25], s[38:39], 11
	s_ashr_i32 s49, s48, 31
	s_add_i32 s40, s0, s26
	global_load_dwordx4 v[26:29], v[2:3], off offset:16
	global_load_dwordx4 v[30:33], v[2:3], off
	v_lshl_add_u64 v[2:3], v[66:67], 0, s[24:25]
	s_lshl_b64 s[24:25], s[48:49], 11
	s_ashr_i32 s41, s40, 31
	global_load_dwordx4 v[18:21], v[2:3], off offset:16
	global_load_dwordx4 v[22:25], v[2:3], off
	v_lshl_add_u64 v[2:3], v[66:67], 0, s[24:25]
	s_lshl_b64 s[24:25], s[40:41], 11
	v_lshl_add_u64 v[6:7], v[66:67], 0, s[24:25]
	global_load_dwordx4 v[10:13], v[2:3], off offset:16
	global_load_dwordx4 v[14:17], v[2:3], off
	s_nop 0
	global_load_dwordx4 v[2:5], v[6:7], off offset:16
	s_nop 0
	global_load_dwordx4 v[6:9], v[6:7], off
	s_and_saveexec_b64 s[24:25], s[4:5]
	s_cbranch_execz .LBB0_224
	s_waitcnt vmcnt(16)
	v_mov_b32_e32 v84, v81
	v_mov_b32_e32 v85, v82
	v_mov_b32_e32 v81, v83
	v_pk_add_f32 v[80:81], v[84:85], v[80:81]
	s_nop 0
	v_add_f32_e32 v73, v80, v81
